# unit-decode fast path also in the QKV, layer-0 per-layer-embedding gate and Wo GEMM loops
# baseline (speedup 1.0000x reference)
.LBB0_1775:
	s_ashr_i32 s8, s44, 3
	s_add_i32 s8, s46, s8
	s_ashr_i32 s9, s8, 31
	s_lshr_b32 s9, s9, 27
	s_add_i32 s9, s8, s9
	s_ashr_i32 s44, s9, 5
	s_lshl_b32 s45, s44, 3
	s_sub_i32 s44, 0x100, s45
	s_min_i32 s46, s44, 8
	s_cmp_eq_u32 s46, 8
	s_cbranch_scc0 .Ldecs_pg0
	s_andn2_b32 s9, s9, 31
	s_sub_i32 s8, s8, s9
	s_lshr_b32 s44, s8, 3
	s_and_b32 s8, s8, 7
	s_branch .Ldecj_pg0
.Ldecs_pg0:
	s_abs_i32 s44, s46
	v_cvt_f32_u32_e32 v18, s44
	s_sub_i32 s48, 0, s44
	s_andn2_b32 s9, s9, 31
	s_sub_i32 s8, s8, s9
	v_rcp_iflag_f32_e32 v18, v18
	s_abs_i32 s9, s8
	s_xor_b32 s47, s8, s46
	s_ashr_i32 s47, s47, 31
	v_mul_f32_e32 v18, 0x4f7ffffe, v18
	v_cvt_u32_f32_e32 v18, v18
	s_nop 0
	v_readfirstlane_b32 s49, v18
	s_mul_i32 s48, s48, s49
	s_mul_hi_u32 s48, s49, s48
	s_add_i32 s49, s49, s48
	s_mul_hi_u32 s48, s9, s49
	s_mul_i32 s49, s48, s44
	s_sub_i32 s9, s9, s49
	s_add_i32 s50, s48, 1
	s_sub_i32 s49, s9, s44
	s_cmp_ge_u32 s9, s44
	s_cselect_b32 s48, s50, s48
	s_cselect_b32 s9, s49, s9
	s_add_i32 s49, s48, 1
	s_cmp_ge_u32 s9, s44
	s_cselect_b32 s9, s49, s48
	s_xor_b32 s9, s9, s47
	s_sub_i32 s44, s9, s47
	s_mul_i32 s9, s44, s46
	s_sub_i32 s8, s8, s9
.Ldecj_pg0:
	s_add_i32 s46, s45, s8

.LBB0_1844:
	v_cmp_gt_i64_e32 vcc, s[30:31], v[158:159]
	v_cmp_lt_i64_e64 s[10:11], s[30:31], v[156:157]
	s_cbranch_vccnz .LBB0_1846
	s_ashr_i32 s13, s30, 31
	s_lshr_b32 s13, s13, 29
	s_add_i32 s13, s30, s13
	s_ashr_i32 s14, s13, 3
	s_and_b32 s13, s13, -8
	s_sub_i32 s13, s30, s13
	s_cmp_lt_i32 s13, 0
	s_movk_i32 s15, 0x1a1
	s_cselect_b32 s15, s15, 0x1a0
	s_mul_i32 s13, s13, s15
	s_add_i32 s13, s13, s14
	s_mul_hi_i32 s14, s13, 0x4ec4ec4f
	s_lshr_b32 s15, s14, 31
	s_ashr_i32 s14, s14, 5
	s_add_i32 s14, s14, s15
	s_lshl_b32 s15, s14, 3
	s_sub_i32 s16, 0x100, s15
	s_min_i32 s16, s16, 8
	s_cmp_eq_u32 s16, 8
	s_cbranch_scc0 .Ldecs_qkv
	s_mulk_i32 s14, 0x68
	s_sub_i32 s13, s13, s14
	s_lshr_b32 s48, s13, 3
	s_and_b32 s13, s13, 7
	s_branch .Ldecj_qkv
.Ldecs_qkv:
	s_abs_i32 s17, s16
	v_cvt_f32_u32_e32 v2, s17
	s_sub_i32 s48, 0, s17
	s_mulk_i32 s14, 0x68
	s_sub_i32 s13, s13, s14
	v_rcp_iflag_f32_e32 v2, v2
	s_abs_i32 s14, s13
	s_xor_b32 s19, s13, s16
	s_ashr_i32 s19, s19, 31
	v_mul_f32_e32 v2, 0x4f7ffffe, v2
	v_cvt_u32_f32_e32 v2, v2
	s_nop 0
	v_readfirstlane_b32 s49, v2
	s_mul_i32 s48, s48, s49
	s_mul_hi_u32 s48, s49, s48
	s_add_i32 s49, s49, s48
	s_mul_hi_u32 s48, s14, s49
	s_mul_i32 s49, s48, s17
	s_sub_i32 s14, s14, s49
	s_add_i32 s50, s48, 1
	s_sub_i32 s49, s14, s17
	s_cmp_ge_u32 s14, s17
	s_cselect_b32 s48, s50, s48
	s_cselect_b32 s14, s49, s14
	s_add_i32 s49, s48, 1
	s_cmp_ge_u32 s14, s17
	s_cselect_b32 s14, s49, s48
	s_xor_b32 s14, s14, s19
	s_sub_i32 s48, s14, s19
	s_mul_i32 s14, s48, s16
	s_sub_i32 s13, s13, s14
.Ldecj_qkv:
	s_add_i32 s50, s15, s13

.LBB0_2297:
	s_ashr_i32 s10, s38, 3
	s_add_i32 s10, s40, s10
	s_ashr_i32 s11, s10, 31
	s_lshr_b32 s11, s11, 27
	s_add_i32 s11, s10, s11
	s_ashr_i32 s38, s11, 5
	s_lshl_b32 s39, s38, 3
	s_sub_i32 s38, 0x100, s39
	s_min_i32 s40, s38, 8
	s_cmp_eq_u32 s40, 8
	s_cbranch_scc0 .Ldecs_wo
	s_andn2_b32 s11, s11, 31
	s_sub_i32 s10, s10, s11
	s_lshr_b32 s38, s10, 3
	s_and_b32 s10, s10, 7
	s_branch .Ldecj_wo
.Ldecs_wo:
	s_abs_i32 s38, s40
	v_cvt_f32_u32_e32 v2, s38
	s_sub_i32 s42, 0, s38
	s_andn2_b32 s11, s11, 31
	s_sub_i32 s10, s10, s11
	v_rcp_iflag_f32_e32 v2, v2
	s_abs_i32 s11, s10
	s_xor_b32 s41, s10, s40
	s_ashr_i32 s41, s41, 31
	v_mul_f32_e32 v2, 0x4f7ffffe, v2
	v_cvt_u32_f32_e32 v2, v2
	s_nop 0
	v_readfirstlane_b32 s43, v2
	s_mul_i32 s42, s42, s43
	s_mul_hi_u32 s42, s43, s42
	s_add_i32 s43, s43, s42
	s_mul_hi_u32 s42, s11, s43
	s_mul_i32 s43, s42, s38
	s_sub_i32 s11, s11, s43
	s_add_i32 s44, s42, 1
	s_sub_i32 s43, s11, s38
	s_cmp_ge_u32 s11, s38
	s_cselect_b32 s42, s44, s42
	s_cselect_b32 s11, s43, s11
	s_add_i32 s43, s42, 1
	s_cmp_ge_u32 s11, s38
	s_cselect_b32 s11, s43, s42
	s_xor_b32 s11, s11, s41
	s_sub_i32 s38, s11, s41
	s_mul_i32 s11, s38, s40
	s_sub_i32 s10, s10, s11
.Ldecj_wo:
	s_add_i32 s40, s39, s10
